# router logits loop unrolled with next-trip loads prefetched (both layers)
# speedup vs baseline: 1.0082x; 1.0082x over previous
.LBB0_1037:
	v_lshl_add_u64 v[72:73], v[34:35], 0, s[8:9]
	global_load_dwordx4 v[180:183], v[36:37], off offset:-256
	global_load_dwordx2 v[212:213], v[72:73], off offset:-128
	global_load_dwordx4 v[184:187], v[36:37], off offset:-192
	global_load_dwordx2 v[214:215], v[72:73], off offset:-96
	global_load_dwordx4 v[188:191], v[36:37], off offset:-128
	global_load_dwordx2 v[216:217], v[72:73], off offset:-64
	global_load_dwordx4 v[192:195], v[36:37], off offset:-64
	global_load_dwordx2 v[218:219], v[72:73], off offset:-32
	global_load_dwordx4 v[196:199], v[36:37], off offset:0
	global_load_dwordx2 v[220:221], v[72:73], off offset:0
	global_load_dwordx4 v[200:203], v[36:37], off offset:64
	global_load_dwordx2 v[222:223], v[72:73], off offset:32
	global_load_dwordx4 v[204:207], v[36:37], off offset:128
	global_load_dwordx2 v[224:225], v[72:73], off offset:64
	global_load_dwordx4 v[208:211], v[36:37], off offset:192
	global_load_dwordx2 v[226:227], v[72:73], off offset:96
	s_add_u32 s8, s8, 0x100
	s_addc_u32 s9, s9, 0
	v_lshl_add_u64 v[72:73], v[34:35], 0, s[8:9]
	v_lshl_add_u64 v[36:37], v[36:37], 0, s[6:7]
	global_load_dwordx4 v[100:103], v[36:37], off offset:-256
	global_load_dwordx2 v[228:229], v[72:73], off offset:-128
	global_load_dwordx4 v[104:107], v[36:37], off offset:-192
	global_load_dwordx2 v[230:231], v[72:73], off offset:-96
	global_load_dwordx4 v[108:111], v[36:37], off offset:-128
	global_load_dwordx2 v[232:233], v[72:73], off offset:-64
	global_load_dwordx4 v[112:115], v[36:37], off offset:-64
	global_load_dwordx2 v[234:235], v[72:73], off offset:-32
	global_load_dwordx4 v[116:119], v[36:37], off offset:0
	global_load_dwordx2 v[236:237], v[72:73], off offset:0
	global_load_dwordx4 v[120:123], v[36:37], off offset:64
	global_load_dwordx2 v[238:239], v[72:73], off offset:32
	global_load_dwordx4 v[124:127], v[36:37], off offset:128
	global_load_dwordx2 v[240:241], v[72:73], off offset:64
	global_load_dwordx4 v[128:131], v[36:37], off offset:192
	global_load_dwordx2 v[242:243], v[72:73], off offset:96
	s_waitcnt vmcnt(30)
	v_lshlrev_b32_e32 v78, 16, v212
	v_and_b32_e32 v80, 0xffff0000, v212
	v_lshlrev_b32_e32 v79, 16, v213
	v_and_b32_e32 v81, 0xffff0000, v213
	v_mfma_f32_16x16x4_f32 v[18:21], v78, v180, v[18:21]
	v_mul_f32_e32 v82, v80, v80
	v_mul_f32_e32 v83, v81, v81
	v_mfma_f32_16x16x4_f32 v[18:21], v80, v181, v[18:21]
	v_fma_f32 v82, v78, v78, v82
	v_fma_f32 v83, v79, v79, v83
	v_mfma_f32_16x16x4_f32 v[18:21], v79, v182, v[18:21]
	v_add_f32_e32 v59, v82, v83
	v_mfma_f32_16x16x4_f32 v[18:21], v81, v183, v[18:21]
	v_add_f32_e32 v33, v33, v59
	s_waitcnt vmcnt(28)
	v_lshlrev_b32_e32 v78, 16, v214
	v_and_b32_e32 v80, 0xffff0000, v214
	v_lshlrev_b32_e32 v79, 16, v215
	v_and_b32_e32 v81, 0xffff0000, v215
	v_mfma_f32_16x16x4_f32 v[18:21], v78, v184, v[18:21]
	v_mul_f32_e32 v82, v80, v80
	v_mul_f32_e32 v83, v81, v81
	v_mfma_f32_16x16x4_f32 v[18:21], v80, v185, v[18:21]
	v_fma_f32 v82, v78, v78, v82
	v_fma_f32 v83, v79, v79, v83
	v_mfma_f32_16x16x4_f32 v[18:21], v79, v186, v[18:21]
	v_add_f32_e32 v59, v82, v83
	v_mfma_f32_16x16x4_f32 v[18:21], v81, v187, v[18:21]
	v_add_f32_e32 v33, v33, v59
	s_waitcnt vmcnt(26)
	v_lshlrev_b32_e32 v78, 16, v216
	v_and_b32_e32 v80, 0xffff0000, v216
	v_lshlrev_b32_e32 v79, 16, v217
	v_and_b32_e32 v81, 0xffff0000, v217
	v_mfma_f32_16x16x4_f32 v[18:21], v78, v188, v[18:21]
	v_mul_f32_e32 v82, v80, v80
	v_mul_f32_e32 v83, v81, v81
	v_mfma_f32_16x16x4_f32 v[18:21], v80, v189, v[18:21]
	v_fma_f32 v82, v78, v78, v82
	v_fma_f32 v83, v79, v79, v83
	v_mfma_f32_16x16x4_f32 v[18:21], v79, v190, v[18:21]
	v_add_f32_e32 v59, v82, v83
	v_mfma_f32_16x16x4_f32 v[18:21], v81, v191, v[18:21]
	v_add_f32_e32 v33, v33, v59
	s_waitcnt vmcnt(24)
	v_lshlrev_b32_e32 v78, 16, v218
	v_and_b32_e32 v80, 0xffff0000, v218
	v_lshlrev_b32_e32 v79, 16, v219
	v_and_b32_e32 v81, 0xffff0000, v219
	v_mfma_f32_16x16x4_f32 v[18:21], v78, v192, v[18:21]
	v_mul_f32_e32 v82, v80, v80
	v_mul_f32_e32 v83, v81, v81
	v_mfma_f32_16x16x4_f32 v[18:21], v80, v193, v[18:21]
	v_fma_f32 v82, v78, v78, v82
	v_fma_f32 v83, v79, v79, v83
	v_mfma_f32_16x16x4_f32 v[18:21], v79, v194, v[18:21]
	v_add_f32_e32 v59, v82, v83
	v_mfma_f32_16x16x4_f32 v[18:21], v81, v195, v[18:21]
	v_add_f32_e32 v33, v33, v59
	s_waitcnt vmcnt(22)
	v_lshlrev_b32_e32 v78, 16, v220
	v_and_b32_e32 v80, 0xffff0000, v220
	v_lshlrev_b32_e32 v79, 16, v221
	v_and_b32_e32 v81, 0xffff0000, v221
	v_mfma_f32_16x16x4_f32 v[18:21], v78, v196, v[18:21]
	v_mul_f32_e32 v82, v80, v80
	v_mul_f32_e32 v83, v81, v81
	v_mfma_f32_16x16x4_f32 v[18:21], v80, v197, v[18:21]
	v_fma_f32 v82, v78, v78, v82
	v_fma_f32 v83, v79, v79, v83
	v_mfma_f32_16x16x4_f32 v[18:21], v79, v198, v[18:21]
	v_add_f32_e32 v59, v82, v83
	v_mfma_f32_16x16x4_f32 v[18:21], v81, v199, v[18:21]
	v_add_f32_e32 v33, v33, v59
	s_waitcnt vmcnt(20)
	v_lshlrev_b32_e32 v78, 16, v222
	v_and_b32_e32 v80, 0xffff0000, v222
	v_lshlrev_b32_e32 v79, 16, v223
	v_and_b32_e32 v81, 0xffff0000, v223
	v_mfma_f32_16x16x4_f32 v[18:21], v78, v200, v[18:21]
	v_mul_f32_e32 v82, v80, v80
	v_mul_f32_e32 v83, v81, v81
	v_mfma_f32_16x16x4_f32 v[18:21], v80, v201, v[18:21]
	v_fma_f32 v82, v78, v78, v82
	v_fma_f32 v83, v79, v79, v83
	v_mfma_f32_16x16x4_f32 v[18:21], v79, v202, v[18:21]
	v_add_f32_e32 v59, v82, v83
	v_mfma_f32_16x16x4_f32 v[18:21], v81, v203, v[18:21]
	v_add_f32_e32 v33, v33, v59
	s_waitcnt vmcnt(18)
	v_lshlrev_b32_e32 v78, 16, v224
	v_and_b32_e32 v80, 0xffff0000, v224
	v_lshlrev_b32_e32 v79, 16, v225
	v_and_b32_e32 v81, 0xffff0000, v225
	v_mfma_f32_16x16x4_f32 v[18:21], v78, v204, v[18:21]
	v_mul_f32_e32 v82, v80, v80
	v_mul_f32_e32 v83, v81, v81
	v_mfma_f32_16x16x4_f32 v[18:21], v80, v205, v[18:21]
	v_fma_f32 v82, v78, v78, v82
	v_fma_f32 v83, v79, v79, v83
	v_mfma_f32_16x16x4_f32 v[18:21], v79, v206, v[18:21]
	v_add_f32_e32 v59, v82, v83
	v_mfma_f32_16x16x4_f32 v[18:21], v81, v207, v[18:21]
	v_add_f32_e32 v33, v33, v59
	s_waitcnt vmcnt(16)
	v_lshlrev_b32_e32 v78, 16, v226
	v_and_b32_e32 v80, 0xffff0000, v226
	v_lshlrev_b32_e32 v79, 16, v227
	v_and_b32_e32 v81, 0xffff0000, v227
	v_mfma_f32_16x16x4_f32 v[18:21], v78, v208, v[18:21]
	v_mul_f32_e32 v82, v80, v80
	v_mul_f32_e32 v83, v81, v81
	v_mfma_f32_16x16x4_f32 v[18:21], v80, v209, v[18:21]
	v_fma_f32 v82, v78, v78, v82
	v_fma_f32 v83, v79, v79, v83
	v_mfma_f32_16x16x4_f32 v[18:21], v79, v210, v[18:21]
	v_add_f32_e32 v59, v82, v83
	v_mfma_f32_16x16x4_f32 v[18:21], v81, v211, v[18:21]
	v_add_f32_e32 v33, v33, v59
	s_add_u32 s8, s8, 0x100
	s_addc_u32 s9, s9, 0
	v_lshl_add_u64 v[72:73], v[34:35], 0, s[8:9]
	v_lshl_add_u64 v[36:37], v[36:37], 0, s[6:7]
	global_load_dwordx4 v[180:183], v[36:37], off offset:-256
	global_load_dwordx2 v[212:213], v[72:73], off offset:-128
	global_load_dwordx4 v[184:187], v[36:37], off offset:-192
	global_load_dwordx2 v[214:215], v[72:73], off offset:-96
	global_load_dwordx4 v[188:191], v[36:37], off offset:-128
	global_load_dwordx2 v[216:217], v[72:73], off offset:-64
	global_load_dwordx4 v[192:195], v[36:37], off offset:-64
	global_load_dwordx2 v[218:219], v[72:73], off offset:-32
	global_load_dwordx4 v[196:199], v[36:37], off offset:0
	global_load_dwordx2 v[220:221], v[72:73], off offset:0
	global_load_dwordx4 v[200:203], v[36:37], off offset:64
	global_load_dwordx2 v[222:223], v[72:73], off offset:32
	global_load_dwordx4 v[204:207], v[36:37], off offset:128
	global_load_dwordx2 v[224:225], v[72:73], off offset:64
	global_load_dwordx4 v[208:211], v[36:37], off offset:192
	global_load_dwordx2 v[226:227], v[72:73], off offset:96
	s_waitcnt vmcnt(30)
	v_lshlrev_b32_e32 v78, 16, v228
	v_and_b32_e32 v80, 0xffff0000, v228
	v_lshlrev_b32_e32 v79, 16, v229
	v_and_b32_e32 v81, 0xffff0000, v229
	v_mfma_f32_16x16x4_f32 v[18:21], v78, v100, v[18:21]
	v_mul_f32_e32 v82, v80, v80
	v_mul_f32_e32 v83, v81, v81
	v_mfma_f32_16x16x4_f32 v[18:21], v80, v101, v[18:21]
	v_fma_f32 v82, v78, v78, v82
	v_fma_f32 v83, v79, v79, v83
	v_mfma_f32_16x16x4_f32 v[18:21], v79, v102, v[18:21]
	v_add_f32_e32 v59, v82, v83
	v_mfma_f32_16x16x4_f32 v[18:21], v81, v103, v[18:21]
	v_add_f32_e32 v33, v33, v59
	s_waitcnt vmcnt(28)
	v_lshlrev_b32_e32 v78, 16, v230
	v_and_b32_e32 v80, 0xffff0000, v230
	v_lshlrev_b32_e32 v79, 16, v231
	v_and_b32_e32 v81, 0xffff0000, v231
	v_mfma_f32_16x16x4_f32 v[18:21], v78, v104, v[18:21]
	v_mul_f32_e32 v82, v80, v80
	v_mul_f32_e32 v83, v81, v81
	v_mfma_f32_16x16x4_f32 v[18:21], v80, v105, v[18:21]
	v_fma_f32 v82, v78, v78, v82
	v_fma_f32 v83, v79, v79, v83
	v_mfma_f32_16x16x4_f32 v[18:21], v79, v106, v[18:21]
	v_add_f32_e32 v59, v82, v83
	v_mfma_f32_16x16x4_f32 v[18:21], v81, v107, v[18:21]
	v_add_f32_e32 v33, v33, v59
	s_waitcnt vmcnt(26)
	v_lshlrev_b32_e32 v78, 16, v232
	v_and_b32_e32 v80, 0xffff0000, v232
	v_lshlrev_b32_e32 v79, 16, v233
	v_and_b32_e32 v81, 0xffff0000, v233
	v_mfma_f32_16x16x4_f32 v[18:21], v78, v108, v[18:21]
	v_mul_f32_e32 v82, v80, v80
	v_mul_f32_e32 v83, v81, v81
	v_mfma_f32_16x16x4_f32 v[18:21], v80, v109, v[18:21]
	v_fma_f32 v82, v78, v78, v82
	v_fma_f32 v83, v79, v79, v83
	v_mfma_f32_16x16x4_f32 v[18:21], v79, v110, v[18:21]
	v_add_f32_e32 v59, v82, v83
	v_mfma_f32_16x16x4_f32 v[18:21], v81, v111, v[18:21]
	v_add_f32_e32 v33, v33, v59
	s_waitcnt vmcnt(24)
	v_lshlrev_b32_e32 v78, 16, v234
	v_and_b32_e32 v80, 0xffff0000, v234
	v_lshlrev_b32_e32 v79, 16, v235
	v_and_b32_e32 v81, 0xffff0000, v235
	v_mfma_f32_16x16x4_f32 v[18:21], v78, v112, v[18:21]
	v_mul_f32_e32 v82, v80, v80
	v_mul_f32_e32 v83, v81, v81
	v_mfma_f32_16x16x4_f32 v[18:21], v80, v113, v[18:21]
	v_fma_f32 v82, v78, v78, v82
	v_fma_f32 v83, v79, v79, v83
	v_mfma_f32_16x16x4_f32 v[18:21], v79, v114, v[18:21]
	v_add_f32_e32 v59, v82, v83
	v_mfma_f32_16x16x4_f32 v[18:21], v81, v115, v[18:21]
	v_add_f32_e32 v33, v33, v59
	s_waitcnt vmcnt(22)
	v_lshlrev_b32_e32 v78, 16, v236
	v_and_b32_e32 v80, 0xffff0000, v236
	v_lshlrev_b32_e32 v79, 16, v237
	v_and_b32_e32 v81, 0xffff0000, v237
	v_mfma_f32_16x16x4_f32 v[18:21], v78, v116, v[18:21]
	v_mul_f32_e32 v82, v80, v80
	v_mul_f32_e32 v83, v81, v81
	v_mfma_f32_16x16x4_f32 v[18:21], v80, v117, v[18:21]
	v_fma_f32 v82, v78, v78, v82
	v_fma_f32 v83, v79, v79, v83
	v_mfma_f32_16x16x4_f32 v[18:21], v79, v118, v[18:21]
	v_add_f32_e32 v59, v82, v83
	v_mfma_f32_16x16x4_f32 v[18:21], v81, v119, v[18:21]
	v_add_f32_e32 v33, v33, v59
	s_waitcnt vmcnt(20)
	v_lshlrev_b32_e32 v78, 16, v238
	v_and_b32_e32 v80, 0xffff0000, v238
	v_lshlrev_b32_e32 v79, 16, v239
	v_and_b32_e32 v81, 0xffff0000, v239
	v_mfma_f32_16x16x4_f32 v[18:21], v78, v120, v[18:21]
	v_mul_f32_e32 v82, v80, v80
	v_mul_f32_e32 v83, v81, v81
	v_mfma_f32_16x16x4_f32 v[18:21], v80, v121, v[18:21]
	v_fma_f32 v82, v78, v78, v82
	v_fma_f32 v83, v79, v79, v83
	v_mfma_f32_16x16x4_f32 v[18:21], v79, v122, v[18:21]
	v_add_f32_e32 v59, v82, v83
	v_mfma_f32_16x16x4_f32 v[18:21], v81, v123, v[18:21]
	v_add_f32_e32 v33, v33, v59
	s_waitcnt vmcnt(18)
	v_lshlrev_b32_e32 v78, 16, v240
	v_and_b32_e32 v80, 0xffff0000, v240
	v_lshlrev_b32_e32 v79, 16, v241
	v_and_b32_e32 v81, 0xffff0000, v241
	v_mfma_f32_16x16x4_f32 v[18:21], v78, v124, v[18:21]
	v_mul_f32_e32 v82, v80, v80
	v_mul_f32_e32 v83, v81, v81
	v_mfma_f32_16x16x4_f32 v[18:21], v80, v125, v[18:21]
	v_fma_f32 v82, v78, v78, v82
	v_fma_f32 v83, v79, v79, v83
	v_mfma_f32_16x16x4_f32 v[18:21], v79, v126, v[18:21]
	v_add_f32_e32 v59, v82, v83
	v_mfma_f32_16x16x4_f32 v[18:21], v81, v127, v[18:21]
	v_add_f32_e32 v33, v33, v59
	s_waitcnt vmcnt(16)
	v_lshlrev_b32_e32 v78, 16, v242
	v_and_b32_e32 v80, 0xffff0000, v242
	v_lshlrev_b32_e32 v79, 16, v243
	v_and_b32_e32 v81, 0xffff0000, v243
	v_mfma_f32_16x16x4_f32 v[18:21], v78, v128, v[18:21]
	v_mul_f32_e32 v82, v80, v80
	v_mul_f32_e32 v83, v81, v81
	v_mfma_f32_16x16x4_f32 v[18:21], v80, v129, v[18:21]
	v_fma_f32 v82, v78, v78, v82
	v_fma_f32 v83, v79, v79, v83
	v_mfma_f32_16x16x4_f32 v[18:21], v79, v130, v[18:21]
	v_add_f32_e32 v59, v82, v83
	v_mfma_f32_16x16x4_f32 v[18:21], v81, v131, v[18:21]
	v_add_f32_e32 v33, v33, v59
	s_add_u32 s8, s8, 0x100
	s_addc_u32 s9, s9, 0
	v_lshl_add_u64 v[72:73], v[34:35], 0, s[8:9]
	v_lshl_add_u64 v[36:37], v[36:37], 0, s[6:7]
	global_load_dwordx4 v[100:103], v[36:37], off offset:-256
	global_load_dwordx2 v[228:229], v[72:73], off offset:-128
	global_load_dwordx4 v[104:107], v[36:37], off offset:-192
	global_load_dwordx2 v[230:231], v[72:73], off offset:-96
	global_load_dwordx4 v[108:111], v[36:37], off offset:-128
	global_load_dwordx2 v[232:233], v[72:73], off offset:-64
	global_load_dwordx4 v[112:115], v[36:37], off offset:-64
	global_load_dwordx2 v[234:235], v[72:73], off offset:-32
	global_load_dwordx4 v[116:119], v[36:37], off offset:0
	global_load_dwordx2 v[236:237], v[72:73], off offset:0
	global_load_dwordx4 v[120:123], v[36:37], off offset:64
	global_load_dwordx2 v[238:239], v[72:73], off offset:32
	global_load_dwordx4 v[124:127], v[36:37], off offset:128
	global_load_dwordx2 v[240:241], v[72:73], off offset:64
	global_load_dwordx4 v[128:131], v[36:37], off offset:192
	global_load_dwordx2 v[242:243], v[72:73], off offset:96
	s_waitcnt vmcnt(30)
	v_lshlrev_b32_e32 v78, 16, v212
	v_and_b32_e32 v80, 0xffff0000, v212
	v_lshlrev_b32_e32 v79, 16, v213
	v_and_b32_e32 v81, 0xffff0000, v213
	v_mfma_f32_16x16x4_f32 v[18:21], v78, v180, v[18:21]
	v_mul_f32_e32 v82, v80, v80
	v_mul_f32_e32 v83, v81, v81
	v_mfma_f32_16x16x4_f32 v[18:21], v80, v181, v[18:21]
	v_fma_f32 v82, v78, v78, v82
	v_fma_f32 v83, v79, v79, v83
	v_mfma_f32_16x16x4_f32 v[18:21], v79, v182, v[18:21]
	v_add_f32_e32 v59, v82, v83
	v_mfma_f32_16x16x4_f32 v[18:21], v81, v183, v[18:21]
	v_add_f32_e32 v33, v33, v59
	s_waitcnt vmcnt(28)
	v_lshlrev_b32_e32 v78, 16, v214
	v_and_b32_e32 v80, 0xffff0000, v214
	v_lshlrev_b32_e32 v79, 16, v215
	v_and_b32_e32 v81, 0xffff0000, v215
	v_mfma_f32_16x16x4_f32 v[18:21], v78, v184, v[18:21]
	v_mul_f32_e32 v82, v80, v80
	v_mul_f32_e32 v83, v81, v81
	v_mfma_f32_16x16x4_f32 v[18:21], v80, v185, v[18:21]
	v_fma_f32 v82, v78, v78, v82
	v_fma_f32 v83, v79, v79, v83
	v_mfma_f32_16x16x4_f32 v[18:21], v79, v186, v[18:21]
	v_add_f32_e32 v59, v82, v83
	v_mfma_f32_16x16x4_f32 v[18:21], v81, v187, v[18:21]
	v_add_f32_e32 v33, v33, v59
	s_waitcnt vmcnt(26)
	v_lshlrev_b32_e32 v78, 16, v216
	v_and_b32_e32 v80, 0xffff0000, v216
	v_lshlrev_b32_e32 v79, 16, v217
	v_and_b32_e32 v81, 0xffff0000, v217
	v_mfma_f32_16x16x4_f32 v[18:21], v78, v188, v[18:21]
	v_mul_f32_e32 v82, v80, v80
	v_mul_f32_e32 v83, v81, v81
	v_mfma_f32_16x16x4_f32 v[18:21], v80, v189, v[18:21]
	v_fma_f32 v82, v78, v78, v82
	v_fma_f32 v83, v79, v79, v83
	v_mfma_f32_16x16x4_f32 v[18:21], v79, v190, v[18:21]
	v_add_f32_e32 v59, v82, v83
	v_mfma_f32_16x16x4_f32 v[18:21], v81, v191, v[18:21]
	v_add_f32_e32 v33, v33, v59
	s_waitcnt vmcnt(24)
	v_lshlrev_b32_e32 v78, 16, v218
	v_and_b32_e32 v80, 0xffff0000, v218
	v_lshlrev_b32_e32 v79, 16, v219
	v_and_b32_e32 v81, 0xffff0000, v219
	v_mfma_f32_16x16x4_f32 v[18:21], v78, v192, v[18:21]
	v_mul_f32_e32 v82, v80, v80
	v_mul_f32_e32 v83, v81, v81
	v_mfma_f32_16x16x4_f32 v[18:21], v80, v193, v[18:21]
	v_fma_f32 v82, v78, v78, v82
	v_fma_f32 v83, v79, v79, v83
	v_mfma_f32_16x16x4_f32 v[18:21], v79, v194, v[18:21]
	v_add_f32_e32 v59, v82, v83
	v_mfma_f32_16x16x4_f32 v[18:21], v81, v195, v[18:21]
	v_add_f32_e32 v33, v33, v59
	s_waitcnt vmcnt(22)
	v_lshlrev_b32_e32 v78, 16, v220
	v_and_b32_e32 v80, 0xffff0000, v220
	v_lshlrev_b32_e32 v79, 16, v221
	v_and_b32_e32 v81, 0xffff0000, v221
	v_mfma_f32_16x16x4_f32 v[18:21], v78, v196, v[18:21]
	v_mul_f32_e32 v82, v80, v80
	v_mul_f32_e32 v83, v81, v81
	v_mfma_f32_16x16x4_f32 v[18:21], v80, v197, v[18:21]
	v_fma_f32 v82, v78, v78, v82
	v_fma_f32 v83, v79, v79, v83
	v_mfma_f32_16x16x4_f32 v[18:21], v79, v198, v[18:21]
	v_add_f32_e32 v59, v82, v83
	v_mfma_f32_16x16x4_f32 v[18:21], v81, v199, v[18:21]
	v_add_f32_e32 v33, v33, v59
	s_waitcnt vmcnt(20)
	v_lshlrev_b32_e32 v78, 16, v222
	v_and_b32_e32 v80, 0xffff0000, v222
	v_lshlrev_b32_e32 v79, 16, v223
	v_and_b32_e32 v81, 0xffff0000, v223
	v_mfma_f32_16x16x4_f32 v[18:21], v78, v200, v[18:21]
	v_mul_f32_e32 v82, v80, v80
	v_mul_f32_e32 v83, v81, v81
	v_mfma_f32_16x16x4_f32 v[18:21], v80, v201, v[18:21]
	v_fma_f32 v82, v78, v78, v82
	v_fma_f32 v83, v79, v79, v83
	v_mfma_f32_16x16x4_f32 v[18:21], v79, v202, v[18:21]
	v_add_f32_e32 v59, v82, v83
	v_mfma_f32_16x16x4_f32 v[18:21], v81, v203, v[18:21]
	v_add_f32_e32 v33, v33, v59
	s_waitcnt vmcnt(18)
	v_lshlrev_b32_e32 v78, 16, v224
	v_and_b32_e32 v80, 0xffff0000, v224
	v_lshlrev_b32_e32 v79, 16, v225
	v_and_b32_e32 v81, 0xffff0000, v225
	v_mfma_f32_16x16x4_f32 v[18:21], v78, v204, v[18:21]
	v_mul_f32_e32 v82, v80, v80
	v_mul_f32_e32 v83, v81, v81
	v_mfma_f32_16x16x4_f32 v[18:21], v80, v205, v[18:21]
	v_fma_f32 v82, v78, v78, v82
	v_fma_f32 v83, v79, v79, v83
	v_mfma_f32_16x16x4_f32 v[18:21], v79, v206, v[18:21]
	v_add_f32_e32 v59, v82, v83
	v_mfma_f32_16x16x4_f32 v[18:21], v81, v207, v[18:21]
	v_add_f32_e32 v33, v33, v59
	s_waitcnt vmcnt(16)
	v_lshlrev_b32_e32 v78, 16, v226
	v_and_b32_e32 v80, 0xffff0000, v226
	v_lshlrev_b32_e32 v79, 16, v227
	v_and_b32_e32 v81, 0xffff0000, v227
	v_mfma_f32_16x16x4_f32 v[18:21], v78, v208, v[18:21]
	v_mul_f32_e32 v82, v80, v80
	v_mul_f32_e32 v83, v81, v81
	v_mfma_f32_16x16x4_f32 v[18:21], v80, v209, v[18:21]
	v_fma_f32 v82, v78, v78, v82
	v_fma_f32 v83, v79, v79, v83
	v_mfma_f32_16x16x4_f32 v[18:21], v79, v210, v[18:21]
	v_add_f32_e32 v59, v82, v83
	v_mfma_f32_16x16x4_f32 v[18:21], v81, v211, v[18:21]
	v_add_f32_e32 v33, v33, v59
	s_waitcnt vmcnt(14)
	v_lshlrev_b32_e32 v78, 16, v228
	v_and_b32_e32 v80, 0xffff0000, v228
	v_lshlrev_b32_e32 v79, 16, v229
	v_and_b32_e32 v81, 0xffff0000, v229
	v_mfma_f32_16x16x4_f32 v[18:21], v78, v100, v[18:21]
	v_mul_f32_e32 v82, v80, v80
	v_mul_f32_e32 v83, v81, v81
	v_mfma_f32_16x16x4_f32 v[18:21], v80, v101, v[18:21]
	v_fma_f32 v82, v78, v78, v82
	v_fma_f32 v83, v79, v79, v83
	v_mfma_f32_16x16x4_f32 v[18:21], v79, v102, v[18:21]
	v_add_f32_e32 v59, v82, v83
	v_mfma_f32_16x16x4_f32 v[18:21], v81, v103, v[18:21]
	v_add_f32_e32 v33, v33, v59
	s_waitcnt vmcnt(12)
	v_lshlrev_b32_e32 v78, 16, v230
	v_and_b32_e32 v80, 0xffff0000, v230
	v_lshlrev_b32_e32 v79, 16, v231
	v_and_b32_e32 v81, 0xffff0000, v231
	v_mfma_f32_16x16x4_f32 v[18:21], v78, v104, v[18:21]
	v_mul_f32_e32 v82, v80, v80
	v_mul_f32_e32 v83, v81, v81
	v_mfma_f32_16x16x4_f32 v[18:21], v80, v105, v[18:21]
	v_fma_f32 v82, v78, v78, v82
	v_fma_f32 v83, v79, v79, v83
	v_mfma_f32_16x16x4_f32 v[18:21], v79, v106, v[18:21]
	v_add_f32_e32 v59, v82, v83
	v_mfma_f32_16x16x4_f32 v[18:21], v81, v107, v[18:21]
	v_add_f32_e32 v33, v33, v59
	s_waitcnt vmcnt(10)
	v_lshlrev_b32_e32 v78, 16, v232
	v_and_b32_e32 v80, 0xffff0000, v232
	v_lshlrev_b32_e32 v79, 16, v233
	v_and_b32_e32 v81, 0xffff0000, v233
	v_mfma_f32_16x16x4_f32 v[18:21], v78, v108, v[18:21]
	v_mul_f32_e32 v82, v80, v80
	v_mul_f32_e32 v83, v81, v81
	v_mfma_f32_16x16x4_f32 v[18:21], v80, v109, v[18:21]
	v_fma_f32 v82, v78, v78, v82
	v_fma_f32 v83, v79, v79, v83
	v_mfma_f32_16x16x4_f32 v[18:21], v79, v110, v[18:21]
	v_add_f32_e32 v59, v82, v83
	v_mfma_f32_16x16x4_f32 v[18:21], v81, v111, v[18:21]
	v_add_f32_e32 v33, v33, v59
	s_waitcnt vmcnt(8)
	v_lshlrev_b32_e32 v78, 16, v234
	v_and_b32_e32 v80, 0xffff0000, v234
	v_lshlrev_b32_e32 v79, 16, v235
	v_and_b32_e32 v81, 0xffff0000, v235
	v_mfma_f32_16x16x4_f32 v[18:21], v78, v112, v[18:21]
	v_mul_f32_e32 v82, v80, v80
	v_mul_f32_e32 v83, v81, v81
	v_mfma_f32_16x16x4_f32 v[18:21], v80, v113, v[18:21]
	v_fma_f32 v82, v78, v78, v82
	v_fma_f32 v83, v79, v79, v83
	v_mfma_f32_16x16x4_f32 v[18:21], v79, v114, v[18:21]
	v_add_f32_e32 v59, v82, v83
	v_mfma_f32_16x16x4_f32 v[18:21], v81, v115, v[18:21]
	v_add_f32_e32 v33, v33, v59
	s_waitcnt vmcnt(6)
	v_lshlrev_b32_e32 v78, 16, v236
	v_and_b32_e32 v80, 0xffff0000, v236
	v_lshlrev_b32_e32 v79, 16, v237
	v_and_b32_e32 v81, 0xffff0000, v237
	v_mfma_f32_16x16x4_f32 v[18:21], v78, v116, v[18:21]
	v_mul_f32_e32 v82, v80, v80
	v_mul_f32_e32 v83, v81, v81
	v_mfma_f32_16x16x4_f32 v[18:21], v80, v117, v[18:21]
	v_fma_f32 v82, v78, v78, v82
	v_fma_f32 v83, v79, v79, v83
	v_mfma_f32_16x16x4_f32 v[18:21], v79, v118, v[18:21]
	v_add_f32_e32 v59, v82, v83
	v_mfma_f32_16x16x4_f32 v[18:21], v81, v119, v[18:21]
	v_add_f32_e32 v33, v33, v59
	s_waitcnt vmcnt(4)
	v_lshlrev_b32_e32 v78, 16, v238
	v_and_b32_e32 v80, 0xffff0000, v238
	v_lshlrev_b32_e32 v79, 16, v239
	v_and_b32_e32 v81, 0xffff0000, v239
	v_mfma_f32_16x16x4_f32 v[18:21], v78, v120, v[18:21]
	v_mul_f32_e32 v82, v80, v80
	v_mul_f32_e32 v83, v81, v81
	v_mfma_f32_16x16x4_f32 v[18:21], v80, v121, v[18:21]
	v_fma_f32 v82, v78, v78, v82
	v_fma_f32 v83, v79, v79, v83
	v_mfma_f32_16x16x4_f32 v[18:21], v79, v122, v[18:21]
	v_add_f32_e32 v59, v82, v83
	v_mfma_f32_16x16x4_f32 v[18:21], v81, v123, v[18:21]
	v_add_f32_e32 v33, v33, v59
	s_waitcnt vmcnt(2)
	v_lshlrev_b32_e32 v78, 16, v240
	v_and_b32_e32 v80, 0xffff0000, v240
	v_lshlrev_b32_e32 v79, 16, v241
	v_and_b32_e32 v81, 0xffff0000, v241
	v_mfma_f32_16x16x4_f32 v[18:21], v78, v124, v[18:21]
	v_mul_f32_e32 v82, v80, v80
	v_mul_f32_e32 v83, v81, v81
	v_mfma_f32_16x16x4_f32 v[18:21], v80, v125, v[18:21]
	v_fma_f32 v82, v78, v78, v82
	v_fma_f32 v83, v79, v79, v83
	v_mfma_f32_16x16x4_f32 v[18:21], v79, v126, v[18:21]
	v_add_f32_e32 v59, v82, v83
	v_mfma_f32_16x16x4_f32 v[18:21], v81, v127, v[18:21]
	v_add_f32_e32 v33, v33, v59
	s_waitcnt vmcnt(0)
	v_lshlrev_b32_e32 v78, 16, v242
	v_and_b32_e32 v80, 0xffff0000, v242
	v_lshlrev_b32_e32 v79, 16, v243
	v_and_b32_e32 v81, 0xffff0000, v243
	v_mfma_f32_16x16x4_f32 v[18:21], v78, v128, v[18:21]
	v_mul_f32_e32 v82, v80, v80
	v_mul_f32_e32 v83, v81, v81
	v_mfma_f32_16x16x4_f32 v[18:21], v80, v129, v[18:21]
	v_fma_f32 v82, v78, v78, v82
	v_fma_f32 v83, v79, v79, v83
	v_mfma_f32_16x16x4_f32 v[18:21], v79, v130, v[18:21]
	v_add_f32_e32 v59, v82, v83
	v_mfma_f32_16x16x4_f32 v[18:21], v81, v131, v[18:21]
	v_add_f32_e32 v33, v33, v59
	s_add_u32 s8, s8, 0x100
	s_addc_u32 s9, s9, 0
	v_lshl_add_u64 v[36:37], v[36:37], 0, s[6:7]
	ds_bpermute_b32 v34, v39, v33
	s_waitcnt lgkmcnt(0)
	s_barrier
	s_nop 5
	ds_write_b128 v41, v[18:21]
	v_add_f32_e32 v33, v33, v34
	ds_bpermute_b32 v34, v40, v33
	s_waitcnt lgkmcnt(0)
	v_add_f32_e32 v33, v33, v34
	s_and_saveexec_b64 s[8:9], s[0:1]
	ds_write_b32 v42, v33 offset:8192
	s_or_b64 exec, exec, s[8:9]
	s_waitcnt lgkmcnt(0)
	s_barrier
	ds_read_b32 v34, v44 offset:8192
	s_waitcnt lgkmcnt(0)
	v_add_f32_e32 v33, v33, v34
	v_fmamk_f32 v33, v33, 0x3a800000, v54
	v_mul_f32_e32 v34, 0x4b800000, v33
	v_cmp_gt_f32_e32 vcc, s11, v33
	s_nop 1
	v_cndmask_b32_e32 v33, v33, v34, vcc
	v_rsq_f32_e32 v33, v33
	ds_read_b128 v[34:37], v43
	v_mul_f32_e32 v59, 0x45800000, v33
	v_cndmask_b32_e32 v33, v33, v59, vcc
	ds_bpermute_b32 v59, v45, v33
	s_waitcnt lgkmcnt(1)
	v_add_f32_e32 v18, v18, v34
	v_add_f32_e32 v19, v19, v35
	v_add_f32_e32 v35, v20, v36
	ds_bpermute_b32 v20, v50, v33
	s_waitcnt lgkmcnt(1)
	v_mul_f32_e32 v34, v18, v59
	ds_bpermute_b32 v60, v46, v34
	v_add_f32_e32 v37, v21, v37
	ds_bpermute_b32 v36, v51, v33
	s_waitcnt lgkmcnt(2)
	v_mul_f32_e32 v21, v19, v20
	ds_bpermute_b32 v62, v46, v21
	s_waitcnt lgkmcnt(2)
	v_max_f32_e32 v60, v60, v60
	v_max_f32_e32 v34, v34, v60
	ds_bpermute_b32 v60, v47, v34
	s_waitcnt lgkmcnt(2)
	v_mul_f32_e32 v61, v35, v36
	s_waitcnt lgkmcnt(1)
	v_max_f32_e32 v62, v62, v62
	v_max_f32_e32 v21, v21, v62
	ds_bpermute_b32 v62, v47, v21
	s_waitcnt lgkmcnt(1)
	v_max_f32_e32 v60, v60, v60
	v_max_f32_e32 v34, v34, v60
	ds_bpermute_b32 v60, v48, v34
	ds_bpermute_b32 v63, v46, v61
	s_waitcnt lgkmcnt(2)
	v_max_f32_e32 v62, v62, v62
	v_max_f32_e32 v21, v21, v62
	ds_bpermute_b32 v62, v48, v21
	s_waitcnt lgkmcnt(2)
	v_max_f32_e32 v60, v60, v60
	v_max_f32_e32 v34, v34, v60
	ds_bpermute_b32 v60, v49, v34
	s_waitcnt lgkmcnt(2)
	v_max_f32_e32 v63, v63, v63
	s_waitcnt lgkmcnt(0)
	v_max_f32_e32 v60, v60, v60
	v_max_f32_e32 v34, v34, v60
	v_fma_f32 v18, v18, v59, -v34
	v_mul_f32_e32 v34, 0x3fb8aa3b, v18
	v_fma_f32 v59, v18, s12, -v34
	v_rndne_f32_e32 v60, v34
	v_fmac_f32_e32 v59, 0x32a5705f, v18
	v_sub_f32_e32 v34, v34, v60
	v_add_f32_e32 v34, v34, v59
	v_cvt_i32_f32_e32 v60, v60
	v_exp_f32_e32 v34, v34
	v_cmp_ngt_f32_e32 vcc, s13, v18
	v_max_f32_e32 v59, v62, v62
	v_max_f32_e32 v21, v21, v59
	v_ldexp_f32 v34, v34, v60
	v_cndmask_b32_e32 v34, 0, v34, vcc
	v_cmp_nlt_f32_e32 vcc, s14, v18
	ds_bpermute_b32 v59, v49, v21
	v_max_f32_e32 v60, v61, v63
	v_cndmask_b32_e32 v18, v57, v34, vcc
	ds_bpermute_b32 v34, v46, v18
	ds_bpermute_b32 v61, v47, v60
	s_waitcnt lgkmcnt(2)
	v_max_f32_e32 v59, v59, v59
	v_max_f32_e32 v21, v21, v59
	v_fma_f32 v21, v19, v20, -v21
	s_waitcnt lgkmcnt(1)
	v_add_f32_e32 v34, v18, v34
	ds_bpermute_b32 v59, v47, v34
	v_mul_f32_e32 v19, 0x3fb8aa3b, v21
	v_fma_f32 v20, v21, s12, -v19
	v_rndne_f32_e32 v62, v19
	v_fmac_f32_e32 v20, 0x32a5705f, v21
	s_waitcnt lgkmcnt(0)
	v_add_f32_e32 v34, v34, v59
	ds_bpermute_b32 v59, v48, v34
	v_sub_f32_e32 v19, v19, v62
	v_add_f32_e32 v19, v19, v20
	v_exp_f32_e32 v63, v19
	v_cmp_ngt_f32_e32 vcc, s13, v21
	s_waitcnt lgkmcnt(0)
	v_add_f32_e32 v19, v34, v59
	v_max_f32_e32 v59, v61, v61
	v_max_f32_e32 v59, v60, v59
	ds_bpermute_b32 v60, v48, v59
	ds_bpermute_b32 v61, v52, v33
	v_cvt_i32_f32_e32 v34, v62
	ds_bpermute_b32 v20, v49, v19
	s_waitcnt lgkmcnt(2)
	v_max_f32_e32 v60, v60, v60
	v_max_f32_e32 v59, v59, v60
	ds_bpermute_b32 v60, v49, v59
	s_waitcnt lgkmcnt(2)
	v_mul_f32_e32 v62, v37, v61
	v_ldexp_f32 v34, v63, v34
	ds_bpermute_b32 v63, v46, v62
	v_cndmask_b32_e32 v34, 0, v34, vcc
	v_cmp_nlt_f32_e32 vcc, s14, v21
	s_nop 1
	v_cndmask_b32_e32 v21, v57, v34, vcc
	s_waitcnt lgkmcnt(1)
	v_max_f32_e32 v34, v60, v60
	v_max_f32_e32 v34, v59, v34
	v_fma_f32 v34, v35, v36, -v34
	s_waitcnt lgkmcnt(0)
	v_max_f32_e32 v35, v63, v63
	v_max_f32_e32 v35, v62, v35
	ds_bpermute_b32 v36, v47, v35
	v_mul_f32_e32 v59, 0x3fb8aa3b, v34
	v_fma_f32 v60, v34, s12, -v59
	v_rndne_f32_e32 v62, v59
	v_fmac_f32_e32 v60, 0x32a5705f, v34
	s_waitcnt lgkmcnt(0)
	v_max_f32_e32 v36, v36, v36
	v_max_f32_e32 v35, v35, v36
	ds_bpermute_b32 v36, v48, v35
	v_sub_f32_e32 v59, v59, v62
	v_add_f32_e32 v59, v59, v60
	v_exp_f32_e32 v59, v59
	v_cvt_i32_f32_e32 v60, v62
	s_waitcnt lgkmcnt(0)
	v_max_f32_e32 v36, v36, v36
	v_max_f32_e32 v35, v35, v36
	ds_bpermute_b32 v36, v49, v35
	v_ldexp_f32 v59, v59, v60
	v_cmp_ngt_f32_e32 vcc, s13, v34
	ds_bpermute_b32 v62, v46, v21
	s_waitcnt lgkmcnt(1)
	v_max_f32_e32 v36, v36, v36
	v_max_f32_e32 v35, v35, v36
	v_fma_f32 v35, v37, v61, -v35
	v_mul_f32_e32 v36, 0x3fb8aa3b, v35
	v_fma_f32 v37, v35, s12, -v36
	v_rndne_f32_e32 v60, v36
	v_fmac_f32_e32 v37, 0x32a5705f, v35
	v_sub_f32_e32 v36, v36, v60
	v_add_f32_e32 v36, v36, v37
	v_exp_f32_e32 v36, v36
	v_cvt_i32_f32_e32 v37, v60
	v_cndmask_b32_e32 v59, 0, v59, vcc
	v_cmp_nlt_f32_e32 vcc, s14, v34
	v_ldexp_f32 v36, v36, v37
	s_nop 0
	v_cndmask_b32_e32 v34, v57, v59, vcc
	v_cmp_ngt_f32_e32 vcc, s13, v35
	ds_bpermute_b32 v59, v46, v34
	s_waitcnt lgkmcnt(1)
	v_add_f32_e32 v37, v21, v62
	v_cndmask_b32_e32 v36, 0, v36, vcc
	v_cmp_nlt_f32_e32 vcc, s14, v35
	ds_bpermute_b32 v60, v47, v37
	s_waitcnt lgkmcnt(1)
	v_add_f32_e32 v59, v34, v59
	v_cndmask_b32_e32 v35, v57, v36, vcc
	ds_bpermute_b32 v36, v46, v35
	ds_bpermute_b32 v61, v47, v59
	s_waitcnt lgkmcnt(2)
	v_add_f32_e32 v37, v37, v60
	ds_bpermute_b32 v60, v48, v37
	s_waitcnt lgkmcnt(2)
	v_add_f32_e32 v36, v35, v36
	ds_bpermute_b32 v62, v47, v36
	s_waitcnt lgkmcnt(2)
	v_add_f32_e32 v59, v59, v61
	ds_bpermute_b32 v61, v48, v59
	s_waitcnt lgkmcnt(1)
	v_add_f32_e32 v62, v36, v62
	ds_bpermute_b32 v63, v48, v62
	v_add_f32_e32 v36, v37, v60
	s_waitcnt lgkmcnt(1)
	v_add_f32_e32 v59, v59, v61
	ds_bpermute_b32 v37, v49, v36
	ds_bpermute_b32 v60, v49, v59
	s_waitcnt lgkmcnt(2)
	v_add_f32_e32 v61, v62, v63
	ds_bpermute_b32 v62, v49, v61
	s_and_saveexec_b64 s[8:9], s[4:5]
	s_cbranch_execz .LBB0_1042
	s_waitcnt lgkmcnt(0)
	v_add_f32_e32 v61, v61, v62
	v_div_scale_f32 v63, s[16:17], v61, v61, v35
	v_rcp_f32_e32 v64, v63
	v_add_f32_e32 v59, v59, v60
	v_div_scale_f32 v60, s[16:17], v59, v59, v34
	v_fma_f32 v65, -v63, v64, 1.0
	v_fmac_f32_e32 v64, v65, v64
	v_div_scale_f32 v65, vcc, v35, v61, v35
	v_mul_f32_e32 v66, v65, v64
	v_fma_f32 v67, -v63, v66, v65
	v_fmac_f32_e32 v66, v67, v64
	v_fma_f32 v63, -v63, v66, v65
	v_rcp_f32_e32 v65, v60
	v_div_fmas_f32 v63, v63, v64, v66
	v_div_fixup_f32 v35, v63, v61, v35
	v_add_f32_e32 v36, v36, v37
	v_fma_f32 v61, -v60, v65, 1.0
	v_fmac_f32_e32 v65, v61, v65
	v_div_scale_f32 v61, vcc, v34, v59, v34
	v_mul_f32_e32 v63, v61, v65
	v_fma_f32 v64, -v60, v63, v61
	v_fmac_f32_e32 v63, v64, v65
	v_div_scale_f32 v37, s[16:17], v36, v36, v21
	v_fma_f32 v60, -v60, v63, v61
	v_rcp_f32_e32 v61, v37
	v_div_fmas_f32 v60, v60, v65, v63
	v_div_fixup_f32 v34, v60, v59, v34
	v_add_f32_e32 v19, v19, v20
	v_fma_f32 v59, -v37, v61, 1.0
	v_fmac_f32_e32 v61, v59, v61
	v_div_scale_f32 v59, vcc, v21, v36, v21
	v_mul_f32_e32 v60, v59, v61
	v_fma_f32 v63, -v37, v60, v59
	v_fmac_f32_e32 v60, v63, v61
	v_div_scale_f32 v20, s[16:17], v19, v19, v18
	v_fma_f32 v37, -v37, v60, v59
	v_rcp_f32_e32 v59, v20
	v_div_fmas_f32 v37, v37, v61, v60
	v_div_fixup_f32 v36, v37, v36, v21
	v_add_u32_e32 v62, s10, v1
	v_fma_f32 v21, -v20, v59, 1.0
	v_fmac_f32_e32 v59, v21, v59
	v_div_scale_f32 v21, vcc, v18, v19, v18
	v_mul_f32_e32 v37, v21, v59
	v_fma_f32 v60, -v20, v37, v21
	v_fmac_f32_e32 v37, v60, v59
	v_lshl_or_b32 v62, v62, 4, v38
	v_fma_f32 v20, -v20, v37, v21
	v_div_fmas_f32 v20, v20, v59, v37
	v_ashrrev_i32_e32 v63, 31, v62
	v_div_fixup_f32 v37, v20, v19, v18
	v_lshlrev_b64 v[18:19], 6, v[62:63]
	v_or_b32_e32 v18, v18, v55
	v_lshl_add_u64 v[20:21], s[92:93], 0, v[18:19]
	v_lshl_add_u64 v[18:19], s[62:63], 0, v[18:19]
	global_store_dword v[18:19], v56, off
	v_or_b32_e32 v18, 1, v62
	v_ashrrev_i32_e32 v19, 31, v18
	v_lshlrev_b64 v[18:19], 6, v[18:19]
	v_or_b32_e32 v18, v18, v55
	global_store_dword v[20:21], v37, off
	v_lshl_add_u64 v[20:21], s[92:93], 0, v[18:19]
	v_lshl_add_u64 v[18:19], s[62:63], 0, v[18:19]
	global_store_dword v[18:19], v56, off
	v_or_b32_e32 v18, 2, v62
	v_ashrrev_i32_e32 v19, 31, v18
	v_lshlrev_b64 v[18:19], 6, v[18:19]
	v_or_b32_e32 v18, v18, v55
	global_store_dword v[20:21], v36, off
	v_lshl_add_u64 v[20:21], s[92:93], 0, v[18:19]
	v_lshl_add_u64 v[18:19], s[62:63], 0, v[18:19]
	global_store_dword v[18:19], v56, off
	v_or_b32_e32 v18, 3, v62
	v_ashrrev_i32_e32 v19, 31, v18
	v_lshlrev_b64 v[18:19], 6, v[18:19]
	v_or_b32_e32 v18, v18, v55
	global_store_dword v[20:21], v34, off
	v_lshl_add_u64 v[20:21], s[92:93], 0, v[18:19]
	v_lshl_add_u64 v[18:19], s[62:63], 0, v[18:19]
	global_store_dword v[20:21], v35, off
	global_store_dword v[18:19], v56, off

.LBB0_2317:
	v_lshl_add_u64 v[72:73], v[34:35], 0, s[8:9]
	global_load_dwordx4 v[180:183], v[36:37], off offset:-256
	global_load_dwordx2 v[212:213], v[72:73], off offset:-128
	global_load_dwordx4 v[184:187], v[36:37], off offset:-192
	global_load_dwordx2 v[214:215], v[72:73], off offset:-96
	global_load_dwordx4 v[188:191], v[36:37], off offset:-128
	global_load_dwordx2 v[216:217], v[72:73], off offset:-64
	global_load_dwordx4 v[192:195], v[36:37], off offset:-64
	global_load_dwordx2 v[218:219], v[72:73], off offset:-32
	global_load_dwordx4 v[196:199], v[36:37], off offset:0
	global_load_dwordx2 v[220:221], v[72:73], off offset:0
	global_load_dwordx4 v[200:203], v[36:37], off offset:64
	global_load_dwordx2 v[222:223], v[72:73], off offset:32
	global_load_dwordx4 v[204:207], v[36:37], off offset:128
	global_load_dwordx2 v[224:225], v[72:73], off offset:64
	global_load_dwordx4 v[208:211], v[36:37], off offset:192
	global_load_dwordx2 v[226:227], v[72:73], off offset:96
	s_add_u32 s8, s8, 0x100
	s_addc_u32 s9, s9, 0
	v_lshl_add_u64 v[72:73], v[34:35], 0, s[8:9]
	v_lshl_add_u64 v[36:37], v[36:37], 0, s[6:7]
	global_load_dwordx4 v[100:103], v[36:37], off offset:-256
	global_load_dwordx2 v[228:229], v[72:73], off offset:-128
	global_load_dwordx4 v[104:107], v[36:37], off offset:-192
	global_load_dwordx2 v[230:231], v[72:73], off offset:-96
	global_load_dwordx4 v[108:111], v[36:37], off offset:-128
	global_load_dwordx2 v[232:233], v[72:73], off offset:-64
	global_load_dwordx4 v[112:115], v[36:37], off offset:-64
	global_load_dwordx2 v[234:235], v[72:73], off offset:-32
	global_load_dwordx4 v[116:119], v[36:37], off offset:0
	global_load_dwordx2 v[236:237], v[72:73], off offset:0
	global_load_dwordx4 v[120:123], v[36:37], off offset:64
	global_load_dwordx2 v[238:239], v[72:73], off offset:32
	global_load_dwordx4 v[124:127], v[36:37], off offset:128
	global_load_dwordx2 v[240:241], v[72:73], off offset:64
	global_load_dwordx4 v[128:131], v[36:37], off offset:192
	global_load_dwordx2 v[242:243], v[72:73], off offset:96
	s_waitcnt vmcnt(30)
	v_lshlrev_b32_e32 v78, 16, v212
	v_and_b32_e32 v80, 0xffff0000, v212
	v_lshlrev_b32_e32 v79, 16, v213
	v_and_b32_e32 v81, 0xffff0000, v213
	v_mfma_f32_16x16x4_f32 v[18:21], v78, v180, v[18:21]
	v_mul_f32_e32 v82, v80, v80
	v_mul_f32_e32 v83, v81, v81
	v_mfma_f32_16x16x4_f32 v[18:21], v80, v181, v[18:21]
	v_fma_f32 v82, v78, v78, v82
	v_fma_f32 v83, v79, v79, v83
	v_mfma_f32_16x16x4_f32 v[18:21], v79, v182, v[18:21]
	v_add_f32_e32 v59, v82, v83
	v_mfma_f32_16x16x4_f32 v[18:21], v81, v183, v[18:21]
	v_add_f32_e32 v33, v33, v59
	s_waitcnt vmcnt(28)
	v_lshlrev_b32_e32 v78, 16, v214
	v_and_b32_e32 v80, 0xffff0000, v214
	v_lshlrev_b32_e32 v79, 16, v215
	v_and_b32_e32 v81, 0xffff0000, v215
	v_mfma_f32_16x16x4_f32 v[18:21], v78, v184, v[18:21]
	v_mul_f32_e32 v82, v80, v80
	v_mul_f32_e32 v83, v81, v81
	v_mfma_f32_16x16x4_f32 v[18:21], v80, v185, v[18:21]
	v_fma_f32 v82, v78, v78, v82
	v_fma_f32 v83, v79, v79, v83
	v_mfma_f32_16x16x4_f32 v[18:21], v79, v186, v[18:21]
	v_add_f32_e32 v59, v82, v83
	v_mfma_f32_16x16x4_f32 v[18:21], v81, v187, v[18:21]
	v_add_f32_e32 v33, v33, v59
	s_waitcnt vmcnt(26)
	v_lshlrev_b32_e32 v78, 16, v216
	v_and_b32_e32 v80, 0xffff0000, v216
	v_lshlrev_b32_e32 v79, 16, v217
	v_and_b32_e32 v81, 0xffff0000, v217
	v_mfma_f32_16x16x4_f32 v[18:21], v78, v188, v[18:21]
	v_mul_f32_e32 v82, v80, v80
	v_mul_f32_e32 v83, v81, v81
	v_mfma_f32_16x16x4_f32 v[18:21], v80, v189, v[18:21]
	v_fma_f32 v82, v78, v78, v82
	v_fma_f32 v83, v79, v79, v83
	v_mfma_f32_16x16x4_f32 v[18:21], v79, v190, v[18:21]
	v_add_f32_e32 v59, v82, v83
	v_mfma_f32_16x16x4_f32 v[18:21], v81, v191, v[18:21]
	v_add_f32_e32 v33, v33, v59
	s_waitcnt vmcnt(24)
	v_lshlrev_b32_e32 v78, 16, v218
	v_and_b32_e32 v80, 0xffff0000, v218
	v_lshlrev_b32_e32 v79, 16, v219
	v_and_b32_e32 v81, 0xffff0000, v219
	v_mfma_f32_16x16x4_f32 v[18:21], v78, v192, v[18:21]
	v_mul_f32_e32 v82, v80, v80
	v_mul_f32_e32 v83, v81, v81
	v_mfma_f32_16x16x4_f32 v[18:21], v80, v193, v[18:21]
	v_fma_f32 v82, v78, v78, v82
	v_fma_f32 v83, v79, v79, v83
	v_mfma_f32_16x16x4_f32 v[18:21], v79, v194, v[18:21]
	v_add_f32_e32 v59, v82, v83
	v_mfma_f32_16x16x4_f32 v[18:21], v81, v195, v[18:21]
	v_add_f32_e32 v33, v33, v59
	s_waitcnt vmcnt(22)
	v_lshlrev_b32_e32 v78, 16, v220
	v_and_b32_e32 v80, 0xffff0000, v220
	v_lshlrev_b32_e32 v79, 16, v221
	v_and_b32_e32 v81, 0xffff0000, v221
	v_mfma_f32_16x16x4_f32 v[18:21], v78, v196, v[18:21]
	v_mul_f32_e32 v82, v80, v80
	v_mul_f32_e32 v83, v81, v81
	v_mfma_f32_16x16x4_f32 v[18:21], v80, v197, v[18:21]
	v_fma_f32 v82, v78, v78, v82
	v_fma_f32 v83, v79, v79, v83
	v_mfma_f32_16x16x4_f32 v[18:21], v79, v198, v[18:21]
	v_add_f32_e32 v59, v82, v83
	v_mfma_f32_16x16x4_f32 v[18:21], v81, v199, v[18:21]
	v_add_f32_e32 v33, v33, v59
	s_waitcnt vmcnt(20)
	v_lshlrev_b32_e32 v78, 16, v222
	v_and_b32_e32 v80, 0xffff0000, v222
	v_lshlrev_b32_e32 v79, 16, v223
	v_and_b32_e32 v81, 0xffff0000, v223
	v_mfma_f32_16x16x4_f32 v[18:21], v78, v200, v[18:21]
	v_mul_f32_e32 v82, v80, v80
	v_mul_f32_e32 v83, v81, v81
	v_mfma_f32_16x16x4_f32 v[18:21], v80, v201, v[18:21]
	v_fma_f32 v82, v78, v78, v82
	v_fma_f32 v83, v79, v79, v83
	v_mfma_f32_16x16x4_f32 v[18:21], v79, v202, v[18:21]
	v_add_f32_e32 v59, v82, v83
	v_mfma_f32_16x16x4_f32 v[18:21], v81, v203, v[18:21]
	v_add_f32_e32 v33, v33, v59
	s_waitcnt vmcnt(18)
	v_lshlrev_b32_e32 v78, 16, v224
	v_and_b32_e32 v80, 0xffff0000, v224
	v_lshlrev_b32_e32 v79, 16, v225
	v_and_b32_e32 v81, 0xffff0000, v225
	v_mfma_f32_16x16x4_f32 v[18:21], v78, v204, v[18:21]
	v_mul_f32_e32 v82, v80, v80
	v_mul_f32_e32 v83, v81, v81
	v_mfma_f32_16x16x4_f32 v[18:21], v80, v205, v[18:21]
	v_fma_f32 v82, v78, v78, v82
	v_fma_f32 v83, v79, v79, v83
	v_mfma_f32_16x16x4_f32 v[18:21], v79, v206, v[18:21]
	v_add_f32_e32 v59, v82, v83
	v_mfma_f32_16x16x4_f32 v[18:21], v81, v207, v[18:21]
	v_add_f32_e32 v33, v33, v59
	s_waitcnt vmcnt(16)
	v_lshlrev_b32_e32 v78, 16, v226
	v_and_b32_e32 v80, 0xffff0000, v226
	v_lshlrev_b32_e32 v79, 16, v227
	v_and_b32_e32 v81, 0xffff0000, v227
	v_mfma_f32_16x16x4_f32 v[18:21], v78, v208, v[18:21]
	v_mul_f32_e32 v82, v80, v80
	v_mul_f32_e32 v83, v81, v81
	v_mfma_f32_16x16x4_f32 v[18:21], v80, v209, v[18:21]
	v_fma_f32 v82, v78, v78, v82
	v_fma_f32 v83, v79, v79, v83
	v_mfma_f32_16x16x4_f32 v[18:21], v79, v210, v[18:21]
	v_add_f32_e32 v59, v82, v83
	v_mfma_f32_16x16x4_f32 v[18:21], v81, v211, v[18:21]
	v_add_f32_e32 v33, v33, v59
	s_add_u32 s8, s8, 0x100
	s_addc_u32 s9, s9, 0
	v_lshl_add_u64 v[72:73], v[34:35], 0, s[8:9]
	v_lshl_add_u64 v[36:37], v[36:37], 0, s[6:7]
	global_load_dwordx4 v[180:183], v[36:37], off offset:-256
	global_load_dwordx2 v[212:213], v[72:73], off offset:-128
	global_load_dwordx4 v[184:187], v[36:37], off offset:-192
	global_load_dwordx2 v[214:215], v[72:73], off offset:-96
	global_load_dwordx4 v[188:191], v[36:37], off offset:-128
	global_load_dwordx2 v[216:217], v[72:73], off offset:-64
	global_load_dwordx4 v[192:195], v[36:37], off offset:-64
	global_load_dwordx2 v[218:219], v[72:73], off offset:-32
	global_load_dwordx4 v[196:199], v[36:37], off offset:0
	global_load_dwordx2 v[220:221], v[72:73], off offset:0
	global_load_dwordx4 v[200:203], v[36:37], off offset:64
	global_load_dwordx2 v[222:223], v[72:73], off offset:32
	global_load_dwordx4 v[204:207], v[36:37], off offset:128
	global_load_dwordx2 v[224:225], v[72:73], off offset:64
	global_load_dwordx4 v[208:211], v[36:37], off offset:192
	global_load_dwordx2 v[226:227], v[72:73], off offset:96
	s_waitcnt vmcnt(30)
	v_lshlrev_b32_e32 v78, 16, v228
	v_and_b32_e32 v80, 0xffff0000, v228
	v_lshlrev_b32_e32 v79, 16, v229
	v_and_b32_e32 v81, 0xffff0000, v229
	v_mfma_f32_16x16x4_f32 v[18:21], v78, v100, v[18:21]
	v_mul_f32_e32 v82, v80, v80
	v_mul_f32_e32 v83, v81, v81
	v_mfma_f32_16x16x4_f32 v[18:21], v80, v101, v[18:21]
	v_fma_f32 v82, v78, v78, v82
	v_fma_f32 v83, v79, v79, v83
	v_mfma_f32_16x16x4_f32 v[18:21], v79, v102, v[18:21]
	v_add_f32_e32 v59, v82, v83
	v_mfma_f32_16x16x4_f32 v[18:21], v81, v103, v[18:21]
	v_add_f32_e32 v33, v33, v59
	s_waitcnt vmcnt(28)
	v_lshlrev_b32_e32 v78, 16, v230
	v_and_b32_e32 v80, 0xffff0000, v230
	v_lshlrev_b32_e32 v79, 16, v231
	v_and_b32_e32 v81, 0xffff0000, v231
	v_mfma_f32_16x16x4_f32 v[18:21], v78, v104, v[18:21]
	v_mul_f32_e32 v82, v80, v80
	v_mul_f32_e32 v83, v81, v81
	v_mfma_f32_16x16x4_f32 v[18:21], v80, v105, v[18:21]
	v_fma_f32 v82, v78, v78, v82
	v_fma_f32 v83, v79, v79, v83
	v_mfma_f32_16x16x4_f32 v[18:21], v79, v106, v[18:21]
	v_add_f32_e32 v59, v82, v83
	v_mfma_f32_16x16x4_f32 v[18:21], v81, v107, v[18:21]
	v_add_f32_e32 v33, v33, v59
	s_waitcnt vmcnt(26)
	v_lshlrev_b32_e32 v78, 16, v232
	v_and_b32_e32 v80, 0xffff0000, v232
	v_lshlrev_b32_e32 v79, 16, v233
	v_and_b32_e32 v81, 0xffff0000, v233
	v_mfma_f32_16x16x4_f32 v[18:21], v78, v108, v[18:21]
	v_mul_f32_e32 v82, v80, v80
	v_mul_f32_e32 v83, v81, v81
	v_mfma_f32_16x16x4_f32 v[18:21], v80, v109, v[18:21]
	v_fma_f32 v82, v78, v78, v82
	v_fma_f32 v83, v79, v79, v83
	v_mfma_f32_16x16x4_f32 v[18:21], v79, v110, v[18:21]
	v_add_f32_e32 v59, v82, v83
	v_mfma_f32_16x16x4_f32 v[18:21], v81, v111, v[18:21]
	v_add_f32_e32 v33, v33, v59
	s_waitcnt vmcnt(24)
	v_lshlrev_b32_e32 v78, 16, v234
	v_and_b32_e32 v80, 0xffff0000, v234
	v_lshlrev_b32_e32 v79, 16, v235
	v_and_b32_e32 v81, 0xffff0000, v235
	v_mfma_f32_16x16x4_f32 v[18:21], v78, v112, v[18:21]
	v_mul_f32_e32 v82, v80, v80
	v_mul_f32_e32 v83, v81, v81
	v_mfma_f32_16x16x4_f32 v[18:21], v80, v113, v[18:21]
	v_fma_f32 v82, v78, v78, v82
	v_fma_f32 v83, v79, v79, v83
	v_mfma_f32_16x16x4_f32 v[18:21], v79, v114, v[18:21]
	v_add_f32_e32 v59, v82, v83
	v_mfma_f32_16x16x4_f32 v[18:21], v81, v115, v[18:21]
	v_add_f32_e32 v33, v33, v59
	s_waitcnt vmcnt(22)
	v_lshlrev_b32_e32 v78, 16, v236
	v_and_b32_e32 v80, 0xffff0000, v236
	v_lshlrev_b32_e32 v79, 16, v237
	v_and_b32_e32 v81, 0xffff0000, v237
	v_mfma_f32_16x16x4_f32 v[18:21], v78, v116, v[18:21]
	v_mul_f32_e32 v82, v80, v80
	v_mul_f32_e32 v83, v81, v81
	v_mfma_f32_16x16x4_f32 v[18:21], v80, v117, v[18:21]
	v_fma_f32 v82, v78, v78, v82
	v_fma_f32 v83, v79, v79, v83
	v_mfma_f32_16x16x4_f32 v[18:21], v79, v118, v[18:21]
	v_add_f32_e32 v59, v82, v83
	v_mfma_f32_16x16x4_f32 v[18:21], v81, v119, v[18:21]
	v_add_f32_e32 v33, v33, v59
	s_waitcnt vmcnt(20)
	v_lshlrev_b32_e32 v78, 16, v238
	v_and_b32_e32 v80, 0xffff0000, v238
	v_lshlrev_b32_e32 v79, 16, v239
	v_and_b32_e32 v81, 0xffff0000, v239
	v_mfma_f32_16x16x4_f32 v[18:21], v78, v120, v[18:21]
	v_mul_f32_e32 v82, v80, v80
	v_mul_f32_e32 v83, v81, v81
	v_mfma_f32_16x16x4_f32 v[18:21], v80, v121, v[18:21]
	v_fma_f32 v82, v78, v78, v82
	v_fma_f32 v83, v79, v79, v83
	v_mfma_f32_16x16x4_f32 v[18:21], v79, v122, v[18:21]
	v_add_f32_e32 v59, v82, v83
	v_mfma_f32_16x16x4_f32 v[18:21], v81, v123, v[18:21]
	v_add_f32_e32 v33, v33, v59
	s_waitcnt vmcnt(18)
	v_lshlrev_b32_e32 v78, 16, v240
	v_and_b32_e32 v80, 0xffff0000, v240
	v_lshlrev_b32_e32 v79, 16, v241
	v_and_b32_e32 v81, 0xffff0000, v241
	v_mfma_f32_16x16x4_f32 v[18:21], v78, v124, v[18:21]
	v_mul_f32_e32 v82, v80, v80
	v_mul_f32_e32 v83, v81, v81
	v_mfma_f32_16x16x4_f32 v[18:21], v80, v125, v[18:21]
	v_fma_f32 v82, v78, v78, v82
	v_fma_f32 v83, v79, v79, v83
	v_mfma_f32_16x16x4_f32 v[18:21], v79, v126, v[18:21]
	v_add_f32_e32 v59, v82, v83
	v_mfma_f32_16x16x4_f32 v[18:21], v81, v127, v[18:21]
	v_add_f32_e32 v33, v33, v59
	s_waitcnt vmcnt(16)
	v_lshlrev_b32_e32 v78, 16, v242
	v_and_b32_e32 v80, 0xffff0000, v242
	v_lshlrev_b32_e32 v79, 16, v243
	v_and_b32_e32 v81, 0xffff0000, v243
	v_mfma_f32_16x16x4_f32 v[18:21], v78, v128, v[18:21]
	v_mul_f32_e32 v82, v80, v80
	v_mul_f32_e32 v83, v81, v81
	v_mfma_f32_16x16x4_f32 v[18:21], v80, v129, v[18:21]
	v_fma_f32 v82, v78, v78, v82
	v_fma_f32 v83, v79, v79, v83
	v_mfma_f32_16x16x4_f32 v[18:21], v79, v130, v[18:21]
	v_add_f32_e32 v59, v82, v83
	v_mfma_f32_16x16x4_f32 v[18:21], v81, v131, v[18:21]
	v_add_f32_e32 v33, v33, v59
	s_add_u32 s8, s8, 0x100
	s_addc_u32 s9, s9, 0
	v_lshl_add_u64 v[72:73], v[34:35], 0, s[8:9]
	v_lshl_add_u64 v[36:37], v[36:37], 0, s[6:7]
	global_load_dwordx4 v[100:103], v[36:37], off offset:-256
	global_load_dwordx2 v[228:229], v[72:73], off offset:-128
	global_load_dwordx4 v[104:107], v[36:37], off offset:-192
	global_load_dwordx2 v[230:231], v[72:73], off offset:-96
	global_load_dwordx4 v[108:111], v[36:37], off offset:-128
	global_load_dwordx2 v[232:233], v[72:73], off offset:-64
	global_load_dwordx4 v[112:115], v[36:37], off offset:-64
	global_load_dwordx2 v[234:235], v[72:73], off offset:-32
	global_load_dwordx4 v[116:119], v[36:37], off offset:0
	global_load_dwordx2 v[236:237], v[72:73], off offset:0
	global_load_dwordx4 v[120:123], v[36:37], off offset:64
	global_load_dwordx2 v[238:239], v[72:73], off offset:32
	global_load_dwordx4 v[124:127], v[36:37], off offset:128
	global_load_dwordx2 v[240:241], v[72:73], off offset:64
	global_load_dwordx4 v[128:131], v[36:37], off offset:192
	global_load_dwordx2 v[242:243], v[72:73], off offset:96
	s_waitcnt vmcnt(30)
	v_lshlrev_b32_e32 v78, 16, v212
	v_and_b32_e32 v80, 0xffff0000, v212
	v_lshlrev_b32_e32 v79, 16, v213
	v_and_b32_e32 v81, 0xffff0000, v213
	v_mfma_f32_16x16x4_f32 v[18:21], v78, v180, v[18:21]
	v_mul_f32_e32 v82, v80, v80
	v_mul_f32_e32 v83, v81, v81
	v_mfma_f32_16x16x4_f32 v[18:21], v80, v181, v[18:21]
	v_fma_f32 v82, v78, v78, v82
	v_fma_f32 v83, v79, v79, v83
	v_mfma_f32_16x16x4_f32 v[18:21], v79, v182, v[18:21]
	v_add_f32_e32 v59, v82, v83
	v_mfma_f32_16x16x4_f32 v[18:21], v81, v183, v[18:21]
	v_add_f32_e32 v33, v33, v59
	s_waitcnt vmcnt(28)
	v_lshlrev_b32_e32 v78, 16, v214
	v_and_b32_e32 v80, 0xffff0000, v214
	v_lshlrev_b32_e32 v79, 16, v215
	v_and_b32_e32 v81, 0xffff0000, v215
	v_mfma_f32_16x16x4_f32 v[18:21], v78, v184, v[18:21]
	v_mul_f32_e32 v82, v80, v80
	v_mul_f32_e32 v83, v81, v81
	v_mfma_f32_16x16x4_f32 v[18:21], v80, v185, v[18:21]
	v_fma_f32 v82, v78, v78, v82
	v_fma_f32 v83, v79, v79, v83
	v_mfma_f32_16x16x4_f32 v[18:21], v79, v186, v[18:21]
	v_add_f32_e32 v59, v82, v83
	v_mfma_f32_16x16x4_f32 v[18:21], v81, v187, v[18:21]
	v_add_f32_e32 v33, v33, v59
	s_waitcnt vmcnt(26)
	v_lshlrev_b32_e32 v78, 16, v216
	v_and_b32_e32 v80, 0xffff0000, v216
	v_lshlrev_b32_e32 v79, 16, v217
	v_and_b32_e32 v81, 0xffff0000, v217
	v_mfma_f32_16x16x4_f32 v[18:21], v78, v188, v[18:21]
	v_mul_f32_e32 v82, v80, v80
	v_mul_f32_e32 v83, v81, v81
	v_mfma_f32_16x16x4_f32 v[18:21], v80, v189, v[18:21]
	v_fma_f32 v82, v78, v78, v82
	v_fma_f32 v83, v79, v79, v83
	v_mfma_f32_16x16x4_f32 v[18:21], v79, v190, v[18:21]
	v_add_f32_e32 v59, v82, v83
	v_mfma_f32_16x16x4_f32 v[18:21], v81, v191, v[18:21]
	v_add_f32_e32 v33, v33, v59
	s_waitcnt vmcnt(24)
	v_lshlrev_b32_e32 v78, 16, v218
	v_and_b32_e32 v80, 0xffff0000, v218
	v_lshlrev_b32_e32 v79, 16, v219
	v_and_b32_e32 v81, 0xffff0000, v219
	v_mfma_f32_16x16x4_f32 v[18:21], v78, v192, v[18:21]
	v_mul_f32_e32 v82, v80, v80
	v_mul_f32_e32 v83, v81, v81
	v_mfma_f32_16x16x4_f32 v[18:21], v80, v193, v[18:21]
	v_fma_f32 v82, v78, v78, v82
	v_fma_f32 v83, v79, v79, v83
	v_mfma_f32_16x16x4_f32 v[18:21], v79, v194, v[18:21]
	v_add_f32_e32 v59, v82, v83
	v_mfma_f32_16x16x4_f32 v[18:21], v81, v195, v[18:21]
	v_add_f32_e32 v33, v33, v59
	s_waitcnt vmcnt(22)
	v_lshlrev_b32_e32 v78, 16, v220
	v_and_b32_e32 v80, 0xffff0000, v220
	v_lshlrev_b32_e32 v79, 16, v221
	v_and_b32_e32 v81, 0xffff0000, v221
	v_mfma_f32_16x16x4_f32 v[18:21], v78, v196, v[18:21]
	v_mul_f32_e32 v82, v80, v80
	v_mul_f32_e32 v83, v81, v81
	v_mfma_f32_16x16x4_f32 v[18:21], v80, v197, v[18:21]
	v_fma_f32 v82, v78, v78, v82
	v_fma_f32 v83, v79, v79, v83
	v_mfma_f32_16x16x4_f32 v[18:21], v79, v198, v[18:21]
	v_add_f32_e32 v59, v82, v83
	v_mfma_f32_16x16x4_f32 v[18:21], v81, v199, v[18:21]
	v_add_f32_e32 v33, v33, v59
	s_waitcnt vmcnt(20)
	v_lshlrev_b32_e32 v78, 16, v222
	v_and_b32_e32 v80, 0xffff0000, v222
	v_lshlrev_b32_e32 v79, 16, v223
	v_and_b32_e32 v81, 0xffff0000, v223
	v_mfma_f32_16x16x4_f32 v[18:21], v78, v200, v[18:21]
	v_mul_f32_e32 v82, v80, v80
	v_mul_f32_e32 v83, v81, v81
	v_mfma_f32_16x16x4_f32 v[18:21], v80, v201, v[18:21]
	v_fma_f32 v82, v78, v78, v82
	v_fma_f32 v83, v79, v79, v83
	v_mfma_f32_16x16x4_f32 v[18:21], v79, v202, v[18:21]
	v_add_f32_e32 v59, v82, v83
	v_mfma_f32_16x16x4_f32 v[18:21], v81, v203, v[18:21]
	v_add_f32_e32 v33, v33, v59
	s_waitcnt vmcnt(18)
	v_lshlrev_b32_e32 v78, 16, v224
	v_and_b32_e32 v80, 0xffff0000, v224
	v_lshlrev_b32_e32 v79, 16, v225
	v_and_b32_e32 v81, 0xffff0000, v225
	v_mfma_f32_16x16x4_f32 v[18:21], v78, v204, v[18:21]
	v_mul_f32_e32 v82, v80, v80
	v_mul_f32_e32 v83, v81, v81
	v_mfma_f32_16x16x4_f32 v[18:21], v80, v205, v[18:21]
	v_fma_f32 v82, v78, v78, v82
	v_fma_f32 v83, v79, v79, v83
	v_mfma_f32_16x16x4_f32 v[18:21], v79, v206, v[18:21]
	v_add_f32_e32 v59, v82, v83
	v_mfma_f32_16x16x4_f32 v[18:21], v81, v207, v[18:21]
	v_add_f32_e32 v33, v33, v59
	s_waitcnt vmcnt(16)
	v_lshlrev_b32_e32 v78, 16, v226
	v_and_b32_e32 v80, 0xffff0000, v226
	v_lshlrev_b32_e32 v79, 16, v227
	v_and_b32_e32 v81, 0xffff0000, v227
	v_mfma_f32_16x16x4_f32 v[18:21], v78, v208, v[18:21]
	v_mul_f32_e32 v82, v80, v80
	v_mul_f32_e32 v83, v81, v81
	v_mfma_f32_16x16x4_f32 v[18:21], v80, v209, v[18:21]
	v_fma_f32 v82, v78, v78, v82
	v_fma_f32 v83, v79, v79, v83
	v_mfma_f32_16x16x4_f32 v[18:21], v79, v210, v[18:21]
	v_add_f32_e32 v59, v82, v83
	v_mfma_f32_16x16x4_f32 v[18:21], v81, v211, v[18:21]
	v_add_f32_e32 v33, v33, v59
	s_waitcnt vmcnt(14)
	v_lshlrev_b32_e32 v78, 16, v228
	v_and_b32_e32 v80, 0xffff0000, v228
	v_lshlrev_b32_e32 v79, 16, v229
	v_and_b32_e32 v81, 0xffff0000, v229
	v_mfma_f32_16x16x4_f32 v[18:21], v78, v100, v[18:21]
	v_mul_f32_e32 v82, v80, v80
	v_mul_f32_e32 v83, v81, v81
	v_mfma_f32_16x16x4_f32 v[18:21], v80, v101, v[18:21]
	v_fma_f32 v82, v78, v78, v82
	v_fma_f32 v83, v79, v79, v83
	v_mfma_f32_16x16x4_f32 v[18:21], v79, v102, v[18:21]
	v_add_f32_e32 v59, v82, v83
	v_mfma_f32_16x16x4_f32 v[18:21], v81, v103, v[18:21]
	v_add_f32_e32 v33, v33, v59
	s_waitcnt vmcnt(12)
	v_lshlrev_b32_e32 v78, 16, v230
	v_and_b32_e32 v80, 0xffff0000, v230
	v_lshlrev_b32_e32 v79, 16, v231
	v_and_b32_e32 v81, 0xffff0000, v231
	v_mfma_f32_16x16x4_f32 v[18:21], v78, v104, v[18:21]
	v_mul_f32_e32 v82, v80, v80
	v_mul_f32_e32 v83, v81, v81
	v_mfma_f32_16x16x4_f32 v[18:21], v80, v105, v[18:21]
	v_fma_f32 v82, v78, v78, v82
	v_fma_f32 v83, v79, v79, v83
	v_mfma_f32_16x16x4_f32 v[18:21], v79, v106, v[18:21]
	v_add_f32_e32 v59, v82, v83
	v_mfma_f32_16x16x4_f32 v[18:21], v81, v107, v[18:21]
	v_add_f32_e32 v33, v33, v59
	s_waitcnt vmcnt(10)
	v_lshlrev_b32_e32 v78, 16, v232
	v_and_b32_e32 v80, 0xffff0000, v232
	v_lshlrev_b32_e32 v79, 16, v233
	v_and_b32_e32 v81, 0xffff0000, v233
	v_mfma_f32_16x16x4_f32 v[18:21], v78, v108, v[18:21]
	v_mul_f32_e32 v82, v80, v80
	v_mul_f32_e32 v83, v81, v81
	v_mfma_f32_16x16x4_f32 v[18:21], v80, v109, v[18:21]
	v_fma_f32 v82, v78, v78, v82
	v_fma_f32 v83, v79, v79, v83
	v_mfma_f32_16x16x4_f32 v[18:21], v79, v110, v[18:21]
	v_add_f32_e32 v59, v82, v83
	v_mfma_f32_16x16x4_f32 v[18:21], v81, v111, v[18:21]
	v_add_f32_e32 v33, v33, v59
	s_waitcnt vmcnt(8)
	v_lshlrev_b32_e32 v78, 16, v234
	v_and_b32_e32 v80, 0xffff0000, v234
	v_lshlrev_b32_e32 v79, 16, v235
	v_and_b32_e32 v81, 0xffff0000, v235
	v_mfma_f32_16x16x4_f32 v[18:21], v78, v112, v[18:21]
	v_mul_f32_e32 v82, v80, v80
	v_mul_f32_e32 v83, v81, v81
	v_mfma_f32_16x16x4_f32 v[18:21], v80, v113, v[18:21]
	v_fma_f32 v82, v78, v78, v82
	v_fma_f32 v83, v79, v79, v83
	v_mfma_f32_16x16x4_f32 v[18:21], v79, v114, v[18:21]
	v_add_f32_e32 v59, v82, v83
	v_mfma_f32_16x16x4_f32 v[18:21], v81, v115, v[18:21]
	v_add_f32_e32 v33, v33, v59
	s_waitcnt vmcnt(6)
	v_lshlrev_b32_e32 v78, 16, v236
	v_and_b32_e32 v80, 0xffff0000, v236
	v_lshlrev_b32_e32 v79, 16, v237
	v_and_b32_e32 v81, 0xffff0000, v237
	v_mfma_f32_16x16x4_f32 v[18:21], v78, v116, v[18:21]
	v_mul_f32_e32 v82, v80, v80
	v_mul_f32_e32 v83, v81, v81
	v_mfma_f32_16x16x4_f32 v[18:21], v80, v117, v[18:21]
	v_fma_f32 v82, v78, v78, v82
	v_fma_f32 v83, v79, v79, v83
	v_mfma_f32_16x16x4_f32 v[18:21], v79, v118, v[18:21]
	v_add_f32_e32 v59, v82, v83
	v_mfma_f32_16x16x4_f32 v[18:21], v81, v119, v[18:21]
	v_add_f32_e32 v33, v33, v59
	s_waitcnt vmcnt(4)
	v_lshlrev_b32_e32 v78, 16, v238
	v_and_b32_e32 v80, 0xffff0000, v238
	v_lshlrev_b32_e32 v79, 16, v239
	v_and_b32_e32 v81, 0xffff0000, v239
	v_mfma_f32_16x16x4_f32 v[18:21], v78, v120, v[18:21]
	v_mul_f32_e32 v82, v80, v80
	v_mul_f32_e32 v83, v81, v81
	v_mfma_f32_16x16x4_f32 v[18:21], v80, v121, v[18:21]
	v_fma_f32 v82, v78, v78, v82
	v_fma_f32 v83, v79, v79, v83
	v_mfma_f32_16x16x4_f32 v[18:21], v79, v122, v[18:21]
	v_add_f32_e32 v59, v82, v83
	v_mfma_f32_16x16x4_f32 v[18:21], v81, v123, v[18:21]
	v_add_f32_e32 v33, v33, v59
	s_waitcnt vmcnt(2)
	v_lshlrev_b32_e32 v78, 16, v240
	v_and_b32_e32 v80, 0xffff0000, v240
	v_lshlrev_b32_e32 v79, 16, v241
	v_and_b32_e32 v81, 0xffff0000, v241
	v_mfma_f32_16x16x4_f32 v[18:21], v78, v124, v[18:21]
	v_mul_f32_e32 v82, v80, v80
	v_mul_f32_e32 v83, v81, v81
	v_mfma_f32_16x16x4_f32 v[18:21], v80, v125, v[18:21]
	v_fma_f32 v82, v78, v78, v82
	v_fma_f32 v83, v79, v79, v83
	v_mfma_f32_16x16x4_f32 v[18:21], v79, v126, v[18:21]
	v_add_f32_e32 v59, v82, v83
	v_mfma_f32_16x16x4_f32 v[18:21], v81, v127, v[18:21]
	v_add_f32_e32 v33, v33, v59
	s_waitcnt vmcnt(0)
	v_lshlrev_b32_e32 v78, 16, v242
	v_and_b32_e32 v80, 0xffff0000, v242
	v_lshlrev_b32_e32 v79, 16, v243
	v_and_b32_e32 v81, 0xffff0000, v243
	v_mfma_f32_16x16x4_f32 v[18:21], v78, v128, v[18:21]
	v_mul_f32_e32 v82, v80, v80
	v_mul_f32_e32 v83, v81, v81
	v_mfma_f32_16x16x4_f32 v[18:21], v80, v129, v[18:21]
	v_fma_f32 v82, v78, v78, v82
	v_fma_f32 v83, v79, v79, v83
	v_mfma_f32_16x16x4_f32 v[18:21], v79, v130, v[18:21]
	v_add_f32_e32 v59, v82, v83
	v_mfma_f32_16x16x4_f32 v[18:21], v81, v131, v[18:21]
	v_add_f32_e32 v33, v33, v59
	s_add_u32 s8, s8, 0x100
	s_addc_u32 s9, s9, 0
	v_lshl_add_u64 v[36:37], v[36:37], 0, s[6:7]
	ds_bpermute_b32 v34, v39, v33
	s_waitcnt lgkmcnt(0)
	s_barrier
	s_nop 5
	ds_write_b128 v41, v[18:21]
	v_add_f32_e32 v33, v33, v34
	ds_bpermute_b32 v34, v40, v33
	s_waitcnt lgkmcnt(0)
	v_add_f32_e32 v33, v33, v34
	s_and_saveexec_b64 s[8:9], s[0:1]
	ds_write_b32 v42, v33 offset:8192
	s_or_b64 exec, exec, s[8:9]
	s_waitcnt lgkmcnt(0)
	s_barrier
	ds_read_b32 v34, v44 offset:8192
	s_waitcnt lgkmcnt(0)
	v_add_f32_e32 v33, v33, v34
	v_fmamk_f32 v33, v33, 0x3a800000, v54
	v_mul_f32_e32 v34, 0x4b800000, v33
	v_cmp_gt_f32_e32 vcc, s11, v33
	s_nop 1
	v_cndmask_b32_e32 v33, v33, v34, vcc
	v_rsq_f32_e32 v33, v33
	ds_read_b128 v[34:37], v43
	v_mul_f32_e32 v59, 0x45800000, v33
	v_cndmask_b32_e32 v33, v33, v59, vcc
	ds_bpermute_b32 v59, v45, v33
	s_waitcnt lgkmcnt(1)
	v_add_f32_e32 v18, v18, v34
	v_add_f32_e32 v19, v19, v35
	v_add_f32_e32 v35, v20, v36
	ds_bpermute_b32 v20, v50, v33
	s_waitcnt lgkmcnt(1)
	v_mul_f32_e32 v34, v18, v59
	ds_bpermute_b32 v60, v46, v34
	v_add_f32_e32 v37, v21, v37
	ds_bpermute_b32 v36, v51, v33
	s_waitcnt lgkmcnt(2)
	v_mul_f32_e32 v21, v19, v20
	ds_bpermute_b32 v62, v46, v21
	s_waitcnt lgkmcnt(2)
	v_max_f32_e32 v60, v60, v60
	v_max_f32_e32 v34, v34, v60
	ds_bpermute_b32 v60, v47, v34
	s_waitcnt lgkmcnt(2)
	v_mul_f32_e32 v61, v35, v36
	s_waitcnt lgkmcnt(1)
	v_max_f32_e32 v62, v62, v62
	v_max_f32_e32 v21, v21, v62
	ds_bpermute_b32 v62, v47, v21
	s_waitcnt lgkmcnt(1)
	v_max_f32_e32 v60, v60, v60
	v_max_f32_e32 v34, v34, v60
	ds_bpermute_b32 v60, v48, v34
	ds_bpermute_b32 v63, v46, v61
	s_waitcnt lgkmcnt(2)
	v_max_f32_e32 v62, v62, v62
	v_max_f32_e32 v21, v21, v62
	ds_bpermute_b32 v62, v48, v21
	s_waitcnt lgkmcnt(2)
	v_max_f32_e32 v60, v60, v60
	v_max_f32_e32 v34, v34, v60
	ds_bpermute_b32 v60, v49, v34
	s_waitcnt lgkmcnt(2)
	v_max_f32_e32 v63, v63, v63
	s_waitcnt lgkmcnt(0)
	v_max_f32_e32 v60, v60, v60
	v_max_f32_e32 v34, v34, v60
	v_fma_f32 v18, v18, v59, -v34
	v_mul_f32_e32 v34, 0x3fb8aa3b, v18
	v_fma_f32 v59, v18, s12, -v34
	v_rndne_f32_e32 v60, v34
	v_fmac_f32_e32 v59, 0x32a5705f, v18
	v_sub_f32_e32 v34, v34, v60
	v_add_f32_e32 v34, v34, v59
	v_cvt_i32_f32_e32 v60, v60
	v_exp_f32_e32 v34, v34
	v_cmp_ngt_f32_e32 vcc, s13, v18
	v_max_f32_e32 v59, v62, v62
	v_max_f32_e32 v21, v21, v59
	v_ldexp_f32 v34, v34, v60
	v_cndmask_b32_e32 v34, 0, v34, vcc
	v_cmp_nlt_f32_e32 vcc, s14, v18
	ds_bpermute_b32 v59, v49, v21
	v_max_f32_e32 v60, v61, v63
	v_cndmask_b32_e32 v18, v57, v34, vcc
	ds_bpermute_b32 v34, v46, v18
	ds_bpermute_b32 v61, v47, v60
	s_waitcnt lgkmcnt(2)
	v_max_f32_e32 v59, v59, v59
	v_max_f32_e32 v21, v21, v59
	v_fma_f32 v21, v19, v20, -v21
	s_waitcnt lgkmcnt(1)
	v_add_f32_e32 v34, v18, v34
	ds_bpermute_b32 v59, v47, v34
	v_mul_f32_e32 v19, 0x3fb8aa3b, v21
	v_fma_f32 v20, v21, s12, -v19
	v_rndne_f32_e32 v62, v19
	v_fmac_f32_e32 v20, 0x32a5705f, v21
	s_waitcnt lgkmcnt(0)
	v_add_f32_e32 v34, v34, v59
	ds_bpermute_b32 v59, v48, v34
	v_sub_f32_e32 v19, v19, v62
	v_add_f32_e32 v19, v19, v20
	v_exp_f32_e32 v63, v19
	v_cmp_ngt_f32_e32 vcc, s13, v21
	s_waitcnt lgkmcnt(0)
	v_add_f32_e32 v19, v34, v59
	v_max_f32_e32 v59, v61, v61
	v_max_f32_e32 v59, v60, v59
	ds_bpermute_b32 v60, v48, v59
	ds_bpermute_b32 v61, v52, v33
	v_cvt_i32_f32_e32 v34, v62
	ds_bpermute_b32 v20, v49, v19
	s_waitcnt lgkmcnt(2)
	v_max_f32_e32 v60, v60, v60
	v_max_f32_e32 v59, v59, v60
	ds_bpermute_b32 v60, v49, v59
	s_waitcnt lgkmcnt(2)
	v_mul_f32_e32 v62, v37, v61
	v_ldexp_f32 v34, v63, v34
	ds_bpermute_b32 v63, v46, v62
	v_cndmask_b32_e32 v34, 0, v34, vcc
	v_cmp_nlt_f32_e32 vcc, s14, v21
	s_nop 1
	v_cndmask_b32_e32 v21, v57, v34, vcc
	s_waitcnt lgkmcnt(1)
	v_max_f32_e32 v34, v60, v60
	v_max_f32_e32 v34, v59, v34
	v_fma_f32 v34, v35, v36, -v34
	s_waitcnt lgkmcnt(0)
	v_max_f32_e32 v35, v63, v63
	v_max_f32_e32 v35, v62, v35
	ds_bpermute_b32 v36, v47, v35
	v_mul_f32_e32 v59, 0x3fb8aa3b, v34
	v_fma_f32 v60, v34, s12, -v59
	v_rndne_f32_e32 v62, v59
	v_fmac_f32_e32 v60, 0x32a5705f, v34
	s_waitcnt lgkmcnt(0)
	v_max_f32_e32 v36, v36, v36
	v_max_f32_e32 v35, v35, v36
	ds_bpermute_b32 v36, v48, v35
	v_sub_f32_e32 v59, v59, v62
	v_add_f32_e32 v59, v59, v60
	v_exp_f32_e32 v59, v59
	v_cvt_i32_f32_e32 v60, v62
	s_waitcnt lgkmcnt(0)
	v_max_f32_e32 v36, v36, v36
	v_max_f32_e32 v35, v35, v36
	ds_bpermute_b32 v36, v49, v35
	v_ldexp_f32 v59, v59, v60
	v_cmp_ngt_f32_e32 vcc, s13, v34
	ds_bpermute_b32 v62, v46, v21
	s_waitcnt lgkmcnt(1)
	v_max_f32_e32 v36, v36, v36
	v_max_f32_e32 v35, v35, v36
	v_fma_f32 v35, v37, v61, -v35
	v_mul_f32_e32 v36, 0x3fb8aa3b, v35
	v_fma_f32 v37, v35, s12, -v36
	v_rndne_f32_e32 v60, v36
	v_fmac_f32_e32 v37, 0x32a5705f, v35
	v_sub_f32_e32 v36, v36, v60
	v_add_f32_e32 v36, v36, v37
	v_exp_f32_e32 v36, v36
	v_cvt_i32_f32_e32 v37, v60
	v_cndmask_b32_e32 v59, 0, v59, vcc
	v_cmp_nlt_f32_e32 vcc, s14, v34
	v_ldexp_f32 v36, v36, v37
	s_nop 0
	v_cndmask_b32_e32 v34, v57, v59, vcc
	v_cmp_ngt_f32_e32 vcc, s13, v35
	ds_bpermute_b32 v59, v46, v34
	s_waitcnt lgkmcnt(1)
	v_add_f32_e32 v37, v21, v62
	v_cndmask_b32_e32 v36, 0, v36, vcc
	v_cmp_nlt_f32_e32 vcc, s14, v35
	ds_bpermute_b32 v60, v47, v37
	s_waitcnt lgkmcnt(1)
	v_add_f32_e32 v59, v34, v59
	v_cndmask_b32_e32 v35, v57, v36, vcc
	ds_bpermute_b32 v36, v46, v35
	ds_bpermute_b32 v61, v47, v59
	s_waitcnt lgkmcnt(2)
	v_add_f32_e32 v37, v37, v60
	ds_bpermute_b32 v60, v48, v37
	s_waitcnt lgkmcnt(2)
	v_add_f32_e32 v36, v35, v36
	ds_bpermute_b32 v62, v47, v36
	s_waitcnt lgkmcnt(2)
	v_add_f32_e32 v59, v59, v61
	ds_bpermute_b32 v61, v48, v59
	s_waitcnt lgkmcnt(1)
	v_add_f32_e32 v62, v36, v62
	ds_bpermute_b32 v63, v48, v62
	v_add_f32_e32 v36, v37, v60
	s_waitcnt lgkmcnt(1)
	v_add_f32_e32 v59, v59, v61
	ds_bpermute_b32 v37, v49, v36
	ds_bpermute_b32 v60, v49, v59
	s_waitcnt lgkmcnt(2)
	v_add_f32_e32 v61, v62, v63
	ds_bpermute_b32 v62, v49, v61
	s_and_saveexec_b64 s[8:9], s[4:5]
	s_cbranch_execz .LBB0_2322
	s_waitcnt lgkmcnt(0)
	v_add_f32_e32 v61, v61, v62
	v_div_scale_f32 v63, s[16:17], v61, v61, v35
	v_rcp_f32_e32 v64, v63
	v_add_f32_e32 v59, v59, v60
	v_div_scale_f32 v60, s[16:17], v59, v59, v34
	v_fma_f32 v65, -v63, v64, 1.0
	v_fmac_f32_e32 v64, v65, v64
	v_div_scale_f32 v65, vcc, v35, v61, v35
	v_mul_f32_e32 v66, v65, v64
	v_fma_f32 v67, -v63, v66, v65
	v_fmac_f32_e32 v66, v67, v64
	v_fma_f32 v63, -v63, v66, v65
	v_rcp_f32_e32 v65, v60
	v_div_fmas_f32 v63, v63, v64, v66
	v_div_fixup_f32 v35, v63, v61, v35
	v_add_f32_e32 v36, v36, v37
	v_fma_f32 v61, -v60, v65, 1.0
	v_fmac_f32_e32 v65, v61, v65
	v_div_scale_f32 v61, vcc, v34, v59, v34
	v_mul_f32_e32 v63, v61, v65
	v_fma_f32 v64, -v60, v63, v61
	v_fmac_f32_e32 v63, v64, v65
	v_div_scale_f32 v37, s[16:17], v36, v36, v21
	v_fma_f32 v60, -v60, v63, v61
	v_rcp_f32_e32 v61, v37
	v_div_fmas_f32 v60, v60, v65, v63
	v_div_fixup_f32 v34, v60, v59, v34
	v_add_f32_e32 v19, v19, v20
	v_fma_f32 v59, -v37, v61, 1.0
	v_fmac_f32_e32 v61, v59, v61
	v_div_scale_f32 v59, vcc, v21, v36, v21
	v_mul_f32_e32 v60, v59, v61
	v_fma_f32 v63, -v37, v60, v59
	v_fmac_f32_e32 v60, v63, v61
	v_div_scale_f32 v20, s[16:17], v19, v19, v18
	v_fma_f32 v37, -v37, v60, v59
	v_rcp_f32_e32 v59, v20
	v_div_fmas_f32 v37, v37, v61, v60
	v_div_fixup_f32 v36, v37, v36, v21
	v_add_u32_e32 v62, s10, v1
	v_fma_f32 v21, -v20, v59, 1.0
	v_fmac_f32_e32 v59, v21, v59
	v_div_scale_f32 v21, vcc, v18, v19, v18
	v_mul_f32_e32 v37, v21, v59
	v_fma_f32 v60, -v20, v37, v21
	v_fmac_f32_e32 v37, v60, v59
	v_lshl_or_b32 v62, v62, 4, v38
	v_fma_f32 v20, -v20, v37, v21
	v_div_fmas_f32 v20, v20, v59, v37
	v_ashrrev_i32_e32 v63, 31, v62
	v_div_fixup_f32 v37, v20, v19, v18
	v_lshlrev_b64 v[18:19], 6, v[62:63]
	v_or_b32_e32 v18, v18, v55
	v_lshl_add_u64 v[20:21], s[72:73], 0, v[18:19]
	v_lshl_add_u64 v[18:19], s[62:63], 0, v[18:19]
	global_store_dword v[18:19], v56, off
	v_or_b32_e32 v18, 1, v62
	v_ashrrev_i32_e32 v19, 31, v18
	v_lshlrev_b64 v[18:19], 6, v[18:19]
	v_or_b32_e32 v18, v18, v55
	global_store_dword v[20:21], v37, off
	v_lshl_add_u64 v[20:21], s[72:73], 0, v[18:19]
	v_lshl_add_u64 v[18:19], s[62:63], 0, v[18:19]
	global_store_dword v[18:19], v56, off
	v_or_b32_e32 v18, 2, v62
	v_ashrrev_i32_e32 v19, 31, v18
	v_lshlrev_b64 v[18:19], 6, v[18:19]
	v_or_b32_e32 v18, v18, v55
	global_store_dword v[20:21], v36, off
	v_lshl_add_u64 v[20:21], s[72:73], 0, v[18:19]
	v_lshl_add_u64 v[18:19], s[62:63], 0, v[18:19]
	global_store_dword v[18:19], v56, off
	v_or_b32_e32 v18, 3, v62
	v_ashrrev_i32_e32 v19, 31, v18
	v_lshlrev_b64 v[18:19], 6, v[18:19]
	v_or_b32_e32 v18, v18, v55
	global_store_dword v[20:21], v34, off
	v_lshl_add_u64 v[20:21], s[72:73], 0, v[18:19]
	v_lshl_add_u64 v[18:19], s[62:63], 0, v[18:19]
	global_store_dword v[20:21], v35, off
	global_store_dword v[18:19], v56, off
